# P9 routing: 76 mov_dpp+canonicalize+max triples fused into single v_max_f32_dpp
# speedup vs baseline: 1.0020x; 1.0020x over previous
; template <int CTRL> __device__ __forceinline__ float dppf(float x) { return __builtin_bit_cast(float, __builtin_amdgcn_update_dpp(0, __builtin_bit_cast(int, x), CTRL, 0xF, 0xF, true)); }
; __device__ __forceinline__ void p9_fused4(Frame& F) {
;     ...
;             const float logit = lg[tl * 64 + lane];
;             const float score = 1.f / (1.f + __expf(-logit)), choice = score + rb;
;             float m1 = choice; m1 = fmaxf(m1, dppf<0xB1>(m1)); m1 = fmaxf(m1, dppf<0x4E>(m1)); m1 = fmaxf(m1, dppf<0x141>(m1));
.LBB0_1405:
	v_add_u32_e32 v146, s37, v191
	s_waitcnt lgkmcnt(0)
	s_barrier
	ds_read_b32 v146, v146
	s_waitcnt lgkmcnt(0)
	v_mul_f32_e32 v146, 0xbfb8aa3b, v146
	v_exp_f32_e32 v146, v146
	s_nop 0
	v_add_f32_e32 v146, 1.0, v146
	v_div_scale_f32 v147, s[22:23], v146, v146, 1.0
	v_rcp_f32_e32 v148, v147
	v_div_scale_f32 v149, vcc, 1.0, v146, 1.0
	v_fma_f32 v150, -v147, v148, 1.0
	v_fmac_f32_e32 v148, v150, v148
	v_mul_f32_e32 v150, v149, v148
	v_fma_f32 v151, -v147, v150, v149
	v_fmac_f32_e32 v150, v151, v148
	v_fma_f32 v147, -v147, v150, v149
	v_div_fmas_f32 v147, v147, v148, v150
	v_div_fixup_f32 v146, v147, v146, 1.0
	v_add_f32_e32 v147, v182, v146
	s_nop 1
	v_max_f32_dpp v148, v147, v147 quad_perm:[1,0,3,2] row_mask:0xf bank_mask:0xf bound_ctrl:1


; template <int CTRL> __device__ __forceinline__ float dppf(float x) { return __builtin_bit_cast(float, __builtin_amdgcn_update_dpp(0, __builtin_bit_cast(int, x), CTRL, 0xF, 0xF, true)); }
; __device__ __forceinline__ void p9_fused4(Frame& F) {
;     ...
;             float m1 = choice; m1 = fmaxf(m1, dppf<0xB1>(m1)); m1 = fmaxf(m1, dppf<0x4E>(m1)); m1 = fmaxf(m1, dppf<0x141>(m1));
	s_nop 1
	v_max_f32_dpp v148, v148, v148 quad_perm:[2,3,0,1] row_mask:0xf bank_mask:0xf bound_ctrl:1


; template <int CTRL> __device__ __forceinline__ float dppf(float x) { return __builtin_bit_cast(float, __builtin_amdgcn_update_dpp(0, __builtin_bit_cast(int, x), CTRL, 0xF, 0xF, true)); }
; __device__ __forceinline__ void p9_fused4(Frame& F) {
;     ...
;             float m1 = choice; m1 = fmaxf(m1, dppf<0xB1>(m1)); m1 = fmaxf(m1, dppf<0x4E>(m1)); m1 = fmaxf(m1, dppf<0x141>(m1));
	s_nop 1
	v_max_f32_dpp v148, v148, v148 row_half_mirror row_mask:0xf bank_mask:0xf bound_ctrl:1


; template <int CTRL> __device__ __forceinline__ float dppf(float x) { return __builtin_bit_cast(float, __builtin_amdgcn_update_dpp(0, __builtin_bit_cast(int, x), CTRL, 0xF, 0xF, true)); }
; template <int CTRL> __device__ __forceinline__ int dppi(int x) { return __builtin_amdgcn_update_dpp(0, x, CTRL, 0xF, 0xF, true); }
; __device__ __forceinline__ void p9_fused4(Frame& F) {
;     ...
;             int cand = (choice == m1) ? (lane & 7) : 8; cand = min(cand, dppi<0xB1>(cand)); cand = min(cand, dppi<0x4E>(cand)); cand = min(cand, dppi<0x141>(cand));
;             float m2 = ((lane & 7) == cand) ? -__builtin_inff() : choice; m2 = fmaxf(m2, dppf<0xB1>(m2)); m2 = fmaxf(m2, dppf<0x4E>(m2)); m2 = fmaxf(m2, dppf<0x141>(m2));
	v_cmp_eq_f32_e32 vcc, v147, v148
	s_nop 1
	v_cndmask_b32_e32 v149, 8, v192, vcc
	s_nop 1
	v_min_i32_dpp v149, v149, v149 quad_perm:[1,0,3,2] row_mask:0xf bank_mask:0xf bound_ctrl:1
	s_nop 1
	v_min_i32_dpp v149, v149, v149 quad_perm:[2,3,0,1] row_mask:0xf bank_mask:0xf bound_ctrl:1
	s_nop 1
	v_min_i32_dpp v149, v149, v149 row_half_mirror row_mask:0xf bank_mask:0xf bound_ctrl:1
	v_cmp_ne_u32_e32 vcc, v192, v149
	s_nop 1
	v_cndmask_b32_e32 v149, v211, v147, vcc
	s_nop 1
	v_max_f32_dpp v149, v149, v149 quad_perm:[1,0,3,2] row_mask:0xf bank_mask:0xf bound_ctrl:1


; template <int CTRL> __device__ __forceinline__ float dppf(float x) { return __builtin_bit_cast(float, __builtin_amdgcn_update_dpp(0, __builtin_bit_cast(int, x), CTRL, 0xF, 0xF, true)); }
; __device__ __forceinline__ void p9_fused4(Frame& F) {
;     ...
;             float m2 = ((lane & 7) == cand) ? -__builtin_inff() : choice; m2 = fmaxf(m2, dppf<0xB1>(m2)); m2 = fmaxf(m2, dppf<0x4E>(m2)); m2 = fmaxf(m2, dppf<0x141>(m2));
	s_nop 1
	v_max_f32_dpp v149, v149, v149 quad_perm:[2,3,0,1] row_mask:0xf bank_mask:0xf bound_ctrl:1


; template <int CTRL> __device__ __forceinline__ float dppf(float x) { return __builtin_bit_cast(float, __builtin_amdgcn_update_dpp(0, __builtin_bit_cast(int, x), CTRL, 0xF, 0xF, true)); }
; __device__ __forceinline__ void p9_fused4(Frame& F) {
;     ...
;             float m2 = ((lane & 7) == cand) ? -__builtin_inff() : choice; m2 = fmaxf(m2, dppf<0xB1>(m2)); m2 = fmaxf(m2, dppf<0x4E>(m2)); m2 = fmaxf(m2, dppf<0x141>(m2));
	s_nop 1
	v_max_f32_dpp v149, v149, v149 row_half_mirror row_mask:0xf bank_mask:0xf bound_ctrl:1


; template <int CTRL> __device__ __forceinline__ float dppf(float x) { return __builtin_bit_cast(float, __builtin_amdgcn_update_dpp(0, __builtin_bit_cast(int, x), CTRL, 0xF, 0xF, true)); }
; __device__ __forceinline__ void p9_fused4(Frame& F) {
;     ...
;             const float gs = m1 + m2; const int g = lane >> 3; int rank = 0;
; #pragma unroll
;             for (int gg = 0; gg < 8; ++gg) { const float sgg = __builtin_bit_cast(float, __builtin_amdgcn_readlane(__builtin_bit_cast(int, gs), gg * 8)); rank += (sgg > gs || (sgg == gs && gg < g)) ? 1 : 0; }
;             const float masked = (rank < 4) ? choice : -1e30f;
;             float v = masked, ssum = 0.f; int r = 8;
; #pragma unroll
;             for (int kk = 0; kk < 8; ++kk) {
;                 float m = v; m = fmaxf(m, dppf<0xB1>(m)); m = fmaxf(m, dppf<0x4E>(m)); m = fmaxf(m, dppf<0x141>(m)); m = fmaxf(m, dppf<0x140>(m));
	v_add_f32_e32 v148, v148, v149
	s_nop 0
	v_readlane_b32 s22, v148, 0
	s_nop 1
	v_cmp_gt_f32_e32 vcc, s22, v148
	v_cmp_eq_f32_e64 s[22:23], s22, v148
	s_and_b64 s[22:23], s[22:23], s[6:7]
	s_or_b64 s[22:23], vcc, s[22:23]
	v_cndmask_b32_e64 v149, 0, 1, s[22:23]
	v_readlane_b32 s22, v148, 8
	s_nop 1
	v_cmp_gt_f32_e32 vcc, s22, v148
	v_cmp_eq_f32_e64 s[22:23], s22, v148
	s_and_b64 s[22:23], s[22:23], s[8:9]
	s_or_b64 s[22:23], vcc, s[22:23]
	v_cndmask_b32_e64 v150, 0, 1, s[22:23]
	v_readlane_b32 s22, v148, 16
	s_nop 1
	v_cmp_gt_f32_e32 vcc, s22, v148
	v_cmp_eq_f32_e64 s[22:23], s22, v148
	s_and_b64 s[22:23], s[22:23], s[10:11]
	s_or_b64 s[22:23], vcc, s[22:23]
	v_cndmask_b32_e64 v151, 0, 1, s[22:23]
	v_readlane_b32 s22, v148, 24
	s_nop 1
	v_cmp_gt_f32_e32 vcc, s22, v148
	v_cmp_eq_f32_e64 s[22:23], s22, v148
	s_and_b64 s[22:23], s[22:23], s[12:13]
	s_or_b64 s[22:23], vcc, s[22:23]
	v_cndmask_b32_e64 v152, 0, 1, s[22:23]
	v_readlane_b32 s22, v148, 32
	s_nop 1
	v_cmp_gt_f32_e32 vcc, s22, v148
	v_cmp_eq_f32_e64 s[22:23], s22, v148
	s_and_b64 s[22:23], s[22:23], s[14:15]
	s_or_b64 s[22:23], vcc, s[22:23]
	v_cndmask_b32_e64 v153, 0, 1, s[22:23]
	v_readlane_b32 s22, v148, 40
	s_nop 1
	v_cmp_gt_f32_e32 vcc, s22, v148
	v_cmp_eq_f32_e64 s[22:23], s22, v148
	s_and_b64 s[22:23], s[22:23], s[16:17]
	s_or_b64 s[22:23], vcc, s[22:23]
	v_cndmask_b32_e64 v154, 0, 1, s[22:23]
	v_readlane_b32 s22, v148, 48
	s_nop 1
	v_cmp_gt_f32_e32 vcc, s22, v148
	v_cmp_eq_f32_e64 s[22:23], s22, v148
	s_and_b64 s[22:23], s[18:19], s[22:23]
	s_or_b64 s[22:23], vcc, s[22:23]
	v_cndmask_b32_e64 v155, 0, 1, s[22:23]
	v_readlane_b32 s22, v148, 56
	s_nop 1
	v_cmp_gt_f32_e32 vcc, s22, v148
	s_nop 1
	v_cndmask_b32_e64 v148, 0, 1, vcc
	v_add_u32_e32 v148, v150, v148
	v_add3_u32 v148, v148, v149, v151
	v_add3_u32 v148, v148, v152, v153
	v_add3_u32 v148, v148, v154, v155
	v_cmp_gt_u32_e32 vcc, 4, v148
	s_nop 1
	v_cndmask_b32_e32 v147, v212, v147, vcc
	s_nop 1
	v_max_f32_dpp v148, v147, v147 quad_perm:[1,0,3,2] row_mask:0xf bank_mask:0xf bound_ctrl:1


; template <int CTRL> __device__ __forceinline__ float dppf(float x) { return __builtin_bit_cast(float, __builtin_amdgcn_update_dpp(0, __builtin_bit_cast(int, x), CTRL, 0xF, 0xF, true)); }
; __device__ __forceinline__ void p9_fused4(Frame& F) {
;     ...
;                 float m = v; m = fmaxf(m, dppf<0xB1>(m)); m = fmaxf(m, dppf<0x4E>(m)); m = fmaxf(m, dppf<0x141>(m)); m = fmaxf(m, dppf<0x140>(m));
	s_nop 1
	v_max_f32_dpp v148, v148, v148 quad_perm:[2,3,0,1] row_mask:0xf bank_mask:0xf bound_ctrl:1


; template <int CTRL> __device__ __forceinline__ float dppf(float x) { return __builtin_bit_cast(float, __builtin_amdgcn_update_dpp(0, __builtin_bit_cast(int, x), CTRL, 0xF, 0xF, true)); }
; __device__ __forceinline__ void p9_fused4(Frame& F) {
;     ...
;                 float m = v; m = fmaxf(m, dppf<0xB1>(m)); m = fmaxf(m, dppf<0x4E>(m)); m = fmaxf(m, dppf<0x141>(m)); m = fmaxf(m, dppf<0x140>(m));
	s_nop 1
	v_max_f32_dpp v148, v148, v148 row_half_mirror row_mask:0xf bank_mask:0xf bound_ctrl:1


; template <int CTRL> __device__ __forceinline__ float dppf(float x) { return __builtin_bit_cast(float, __builtin_amdgcn_update_dpp(0, __builtin_bit_cast(int, x), CTRL, 0xF, 0xF, true)); }
; __device__ __forceinline__ void p9_fused4(Frame& F) {
;     ...
;                 float m = v; m = fmaxf(m, dppf<0xB1>(m)); m = fmaxf(m, dppf<0x4E>(m)); m = fmaxf(m, dppf<0x141>(m)); m = fmaxf(m, dppf<0x140>(m));
	s_nop 1
	v_max_f32_dpp v148, v148, v148 row_mirror row_mask:0xf bank_mask:0xf bound_ctrl:1


; template <int CTRL> __device__ __forceinline__ float dppf(float x) { return __builtin_bit_cast(float, __builtin_amdgcn_update_dpp(0, __builtin_bit_cast(int, x), CTRL, 0xF, 0xF, true)); }
; __device__ __forceinline__ void p9_fused4(Frame& F) {
;     ...
;                 float m = v; m = fmaxf(m, dppf<0xB1>(m)); m = fmaxf(m, dppf<0x4E>(m)); m = fmaxf(m, dppf<0x141>(m)); m = fmaxf(m, dppf<0x140>(m));
;                 const float r0 = __builtin_bit_cast(float, __builtin_amdgcn_readlane(__builtin_bit_cast(int, m), 0)), r1 = __builtin_bit_cast(float, __builtin_amdgcn_readlane(__builtin_bit_cast(int, m), 16));
;                 const float r2 = __builtin_bit_cast(float, __builtin_amdgcn_readlane(__builtin_bit_cast(int, m), 32)), r3 = __builtin_bit_cast(float, __builtin_amdgcn_readlane(__builtin_bit_cast(int, m), 48));
;                 const float wm = fmaxf(fmaxf(r0, r1), fmaxf(r2, r3));
;                 const unsigned long long bal = __builtin_amdgcn_ballot_w64(v == wm);
;                 const int selL = (int)__builtin_ctzll(bal);
;                 ssum += __builtin_bit_cast(float, __builtin_amdgcn_readlane(__builtin_bit_cast(int, score), selL));
;                 if (lane == selL) { r = kk; v = -__builtin_inff(); }
	s_nop 0
	v_readlane_b32 s56, v148, 32
	v_readlane_b32 s57, v148, 48
	v_readlane_b32 s22, v148, 0
	v_readlane_b32 s23, v148, 16
	v_max_f32_e64 v148, s57, s57
	v_max_f32_e64 v149, s56, s56
	v_max_f32_e32 v148, v149, v148
	v_mov_b32_e32 v149, s23
	v_max3_f32 v148, s22, v149, v148
	v_cmp_eq_f32_e32 vcc, v147, v148
	s_ff1_i32_b64 s22, vcc
	v_cmp_eq_u32_e32 vcc, s22, v163
	v_readlane_b32 s56, v146, s22
	s_nop 0
	v_cndmask_b32_e32 v147, v147, v211, vcc
	v_cndmask_b32_e64 v148, 8, 0, vcc
	s_nop 0
	v_max_f32_dpp v149, v147, v147 quad_perm:[1,0,3,2] row_mask:0xf bank_mask:0xf bound_ctrl:1


; template <int CTRL> __device__ __forceinline__ float dppf(float x) { return __builtin_bit_cast(float, __builtin_amdgcn_update_dpp(0, __builtin_bit_cast(int, x), CTRL, 0xF, 0xF, true)); }
; __device__ __forceinline__ void p9_fused4(Frame& F) {
;     ...
;                 float m = v; m = fmaxf(m, dppf<0xB1>(m)); m = fmaxf(m, dppf<0x4E>(m)); m = fmaxf(m, dppf<0x141>(m)); m = fmaxf(m, dppf<0x140>(m));
	s_nop 1
	v_max_f32_dpp v149, v149, v149 quad_perm:[2,3,0,1] row_mask:0xf bank_mask:0xf bound_ctrl:1


; template <int CTRL> __device__ __forceinline__ float dppf(float x) { return __builtin_bit_cast(float, __builtin_amdgcn_update_dpp(0, __builtin_bit_cast(int, x), CTRL, 0xF, 0xF, true)); }
; __device__ __forceinline__ void p9_fused4(Frame& F) {
;     ...
;                 float m = v; m = fmaxf(m, dppf<0xB1>(m)); m = fmaxf(m, dppf<0x4E>(m)); m = fmaxf(m, dppf<0x141>(m)); m = fmaxf(m, dppf<0x140>(m));
	s_nop 1
	v_max_f32_dpp v149, v149, v149 row_half_mirror row_mask:0xf bank_mask:0xf bound_ctrl:1


; template <int CTRL> __device__ __forceinline__ float dppf(float x) { return __builtin_bit_cast(float, __builtin_amdgcn_update_dpp(0, __builtin_bit_cast(int, x), CTRL, 0xF, 0xF, true)); }
; __device__ __forceinline__ void p9_fused4(Frame& F) {
;     ...
;                 float m = v; m = fmaxf(m, dppf<0xB1>(m)); m = fmaxf(m, dppf<0x4E>(m)); m = fmaxf(m, dppf<0x141>(m)); m = fmaxf(m, dppf<0x140>(m));
	s_nop 1
	v_max_f32_dpp v149, v149, v149 row_mirror row_mask:0xf bank_mask:0xf bound_ctrl:1


; template <int CTRL> __device__ __forceinline__ float dppf(float x) { return __builtin_bit_cast(float, __builtin_amdgcn_update_dpp(0, __builtin_bit_cast(int, x), CTRL, 0xF, 0xF, true)); }
; __device__ __forceinline__ void p9_fused4(Frame& F) {
;     ...
;                 float m = v; m = fmaxf(m, dppf<0xB1>(m)); m = fmaxf(m, dppf<0x4E>(m)); m = fmaxf(m, dppf<0x141>(m)); m = fmaxf(m, dppf<0x140>(m));
;                 const float r0 = __builtin_bit_cast(float, __builtin_amdgcn_readlane(__builtin_bit_cast(int, m), 0)), r1 = __builtin_bit_cast(float, __builtin_amdgcn_readlane(__builtin_bit_cast(int, m), 16));
;                 const float r2 = __builtin_bit_cast(float, __builtin_amdgcn_readlane(__builtin_bit_cast(int, m), 32)), r3 = __builtin_bit_cast(float, __builtin_amdgcn_readlane(__builtin_bit_cast(int, m), 48));
;                 const float wm = fmaxf(fmaxf(r0, r1), fmaxf(r2, r3));
;                 const unsigned long long bal = __builtin_amdgcn_ballot_w64(v == wm);
;                 const int selL = (int)__builtin_ctzll(bal);
;                 ssum += __builtin_bit_cast(float, __builtin_amdgcn_readlane(__builtin_bit_cast(int, score), selL));
;                 if (lane == selL) { r = kk; v = -__builtin_inff(); }
	s_nop 0
	v_readlane_b32 s57, v149, 32
	v_readlane_b32 s58, v149, 48
	v_readlane_b32 s22, v149, 0
	v_readlane_b32 s23, v149, 16
	v_max_f32_e64 v149, s58, s58
	v_max_f32_e64 v150, s57, s57
	v_max_f32_e32 v149, v150, v149
	v_mov_b32_e32 v150, s23
	v_max3_f32 v149, s22, v150, v149
	v_cmp_eq_f32_e32 vcc, v147, v149
	s_ff1_i32_b64 s22, vcc
	v_cmp_eq_u32_e32 vcc, s22, v163
	v_readlane_b32 s57, v146, s22
	s_nop 0
	v_cndmask_b32_e32 v147, v147, v211, vcc
	v_cndmask_b32_e64 v148, v148, 1, vcc
	s_nop 0
	v_max_f32_dpp v149, v147, v147 quad_perm:[1,0,3,2] row_mask:0xf bank_mask:0xf bound_ctrl:1


; template <int CTRL> __device__ __forceinline__ float dppf(float x) { return __builtin_bit_cast(float, __builtin_amdgcn_update_dpp(0, __builtin_bit_cast(int, x), CTRL, 0xF, 0xF, true)); }
; __device__ __forceinline__ void p9_fused4(Frame& F) {
;     ...
;                 float m = v; m = fmaxf(m, dppf<0xB1>(m)); m = fmaxf(m, dppf<0x4E>(m)); m = fmaxf(m, dppf<0x141>(m)); m = fmaxf(m, dppf<0x140>(m));
	s_nop 1
	v_max_f32_dpp v149, v149, v149 quad_perm:[2,3,0,1] row_mask:0xf bank_mask:0xf bound_ctrl:1


; template <int CTRL> __device__ __forceinline__ float dppf(float x) { return __builtin_bit_cast(float, __builtin_amdgcn_update_dpp(0, __builtin_bit_cast(int, x), CTRL, 0xF, 0xF, true)); }
; __device__ __forceinline__ void p9_fused4(Frame& F) {
;     ...
;                 float m = v; m = fmaxf(m, dppf<0xB1>(m)); m = fmaxf(m, dppf<0x4E>(m)); m = fmaxf(m, dppf<0x141>(m)); m = fmaxf(m, dppf<0x140>(m));
	s_nop 1
	v_max_f32_dpp v149, v149, v149 row_half_mirror row_mask:0xf bank_mask:0xf bound_ctrl:1


; template <int CTRL> __device__ __forceinline__ float dppf(float x) { return __builtin_bit_cast(float, __builtin_amdgcn_update_dpp(0, __builtin_bit_cast(int, x), CTRL, 0xF, 0xF, true)); }
; __device__ __forceinline__ void p9_fused4(Frame& F) {
;     ...
;                 float m = v; m = fmaxf(m, dppf<0xB1>(m)); m = fmaxf(m, dppf<0x4E>(m)); m = fmaxf(m, dppf<0x141>(m)); m = fmaxf(m, dppf<0x140>(m));
	s_nop 1
	v_max_f32_dpp v149, v149, v149 row_mirror row_mask:0xf bank_mask:0xf bound_ctrl:1


; template <int CTRL> __device__ __forceinline__ float dppf(float x) { return __builtin_bit_cast(float, __builtin_amdgcn_update_dpp(0, __builtin_bit_cast(int, x), CTRL, 0xF, 0xF, true)); }
; __device__ __forceinline__ void p9_fused4(Frame& F) {
;     ...
;                 float m = v; m = fmaxf(m, dppf<0xB1>(m)); m = fmaxf(m, dppf<0x4E>(m)); m = fmaxf(m, dppf<0x141>(m)); m = fmaxf(m, dppf<0x140>(m));
;                 const float r0 = __builtin_bit_cast(float, __builtin_amdgcn_readlane(__builtin_bit_cast(int, m), 0)), r1 = __builtin_bit_cast(float, __builtin_amdgcn_readlane(__builtin_bit_cast(int, m), 16));
;                 const float r2 = __builtin_bit_cast(float, __builtin_amdgcn_readlane(__builtin_bit_cast(int, m), 32)), r3 = __builtin_bit_cast(float, __builtin_amdgcn_readlane(__builtin_bit_cast(int, m), 48));
;                 const float wm = fmaxf(fmaxf(r0, r1), fmaxf(r2, r3));
;                 const unsigned long long bal = __builtin_amdgcn_ballot_w64(v == wm);
;                 const int selL = (int)__builtin_ctzll(bal);
;                 ssum += __builtin_bit_cast(float, __builtin_amdgcn_readlane(__builtin_bit_cast(int, score), selL));
;                 if (lane == selL) { r = kk; v = -__builtin_inff(); }
	s_nop 0
	v_readlane_b32 s58, v149, 32
	v_readlane_b32 s59, v149, 48
	v_readlane_b32 s22, v149, 0
	v_readlane_b32 s23, v149, 16
	v_max_f32_e64 v149, s59, s59
	v_max_f32_e64 v150, s58, s58
	v_max_f32_e32 v149, v150, v149
	v_mov_b32_e32 v150, s23
	v_max3_f32 v149, s22, v150, v149
	v_cmp_eq_f32_e32 vcc, v147, v149
	s_ff1_i32_b64 s22, vcc
	v_cmp_eq_u32_e32 vcc, s22, v163
	v_readlane_b32 s58, v146, s22
	s_nop 0
	v_cndmask_b32_e32 v147, v147, v211, vcc
	v_cndmask_b32_e64 v148, v148, 2, vcc
	s_nop 0
	v_max_f32_dpp v149, v147, v147 quad_perm:[1,0,3,2] row_mask:0xf bank_mask:0xf bound_ctrl:1


; template <int CTRL> __device__ __forceinline__ float dppf(float x) { return __builtin_bit_cast(float, __builtin_amdgcn_update_dpp(0, __builtin_bit_cast(int, x), CTRL, 0xF, 0xF, true)); }
; __device__ __forceinline__ void p9_fused4(Frame& F) {
;     ...
;                 float m = v; m = fmaxf(m, dppf<0xB1>(m)); m = fmaxf(m, dppf<0x4E>(m)); m = fmaxf(m, dppf<0x141>(m)); m = fmaxf(m, dppf<0x140>(m));
	s_nop 1
	v_max_f32_dpp v149, v149, v149 quad_perm:[2,3,0,1] row_mask:0xf bank_mask:0xf bound_ctrl:1


; template <int CTRL> __device__ __forceinline__ float dppf(float x) { return __builtin_bit_cast(float, __builtin_amdgcn_update_dpp(0, __builtin_bit_cast(int, x), CTRL, 0xF, 0xF, true)); }
; __device__ __forceinline__ void p9_fused4(Frame& F) {
;     ...
;                 float m = v; m = fmaxf(m, dppf<0xB1>(m)); m = fmaxf(m, dppf<0x4E>(m)); m = fmaxf(m, dppf<0x141>(m)); m = fmaxf(m, dppf<0x140>(m));
	s_nop 1
	v_max_f32_dpp v149, v149, v149 row_half_mirror row_mask:0xf bank_mask:0xf bound_ctrl:1


; template <int CTRL> __device__ __forceinline__ float dppf(float x) { return __builtin_bit_cast(float, __builtin_amdgcn_update_dpp(0, __builtin_bit_cast(int, x), CTRL, 0xF, 0xF, true)); }
; __device__ __forceinline__ void p9_fused4(Frame& F) {
;     ...
;                 float m = v; m = fmaxf(m, dppf<0xB1>(m)); m = fmaxf(m, dppf<0x4E>(m)); m = fmaxf(m, dppf<0x141>(m)); m = fmaxf(m, dppf<0x140>(m));
	s_nop 1
	v_max_f32_dpp v149, v149, v149 row_mirror row_mask:0xf bank_mask:0xf bound_ctrl:1


; template <int CTRL> __device__ __forceinline__ float dppf(float x) { return __builtin_bit_cast(float, __builtin_amdgcn_update_dpp(0, __builtin_bit_cast(int, x), CTRL, 0xF, 0xF, true)); }
; __device__ __forceinline__ void p9_fused4(Frame& F) {
;     ...
;                 float m = v; m = fmaxf(m, dppf<0xB1>(m)); m = fmaxf(m, dppf<0x4E>(m)); m = fmaxf(m, dppf<0x141>(m)); m = fmaxf(m, dppf<0x140>(m));
;                 const float r0 = __builtin_bit_cast(float, __builtin_amdgcn_readlane(__builtin_bit_cast(int, m), 0)), r1 = __builtin_bit_cast(float, __builtin_amdgcn_readlane(__builtin_bit_cast(int, m), 16));
;                 const float r2 = __builtin_bit_cast(float, __builtin_amdgcn_readlane(__builtin_bit_cast(int, m), 32)), r3 = __builtin_bit_cast(float, __builtin_amdgcn_readlane(__builtin_bit_cast(int, m), 48));
;                 const float wm = fmaxf(fmaxf(r0, r1), fmaxf(r2, r3));
;                 const unsigned long long bal = __builtin_amdgcn_ballot_w64(v == wm);
;                 const int selL = (int)__builtin_ctzll(bal);
;                 ssum += __builtin_bit_cast(float, __builtin_amdgcn_readlane(__builtin_bit_cast(int, score), selL));
;                 if (lane == selL) { r = kk; v = -__builtin_inff(); }
	s_nop 0
	v_readlane_b32 s59, v149, 32
	v_readlane_b32 s60, v149, 48
	v_readlane_b32 s22, v149, 0
	v_readlane_b32 s23, v149, 16
	v_max_f32_e64 v149, s60, s60
	v_max_f32_e64 v150, s59, s59
	v_max_f32_e32 v149, v150, v149
	v_mov_b32_e32 v150, s23
	v_max3_f32 v149, s22, v150, v149
	v_cmp_eq_f32_e32 vcc, v147, v149
	s_ff1_i32_b64 s22, vcc
	v_cmp_eq_u32_e32 vcc, s22, v163
	v_readlane_b32 s59, v146, s22
	s_nop 0
	v_cndmask_b32_e32 v147, v147, v211, vcc
	v_cndmask_b32_e64 v148, v148, 3, vcc
	s_nop 0
	v_max_f32_dpp v149, v147, v147 quad_perm:[1,0,3,2] row_mask:0xf bank_mask:0xf bound_ctrl:1


; template <int CTRL> __device__ __forceinline__ float dppf(float x) { return __builtin_bit_cast(float, __builtin_amdgcn_update_dpp(0, __builtin_bit_cast(int, x), CTRL, 0xF, 0xF, true)); }
; __device__ __forceinline__ void p9_fused4(Frame& F) {
;     ...
;                 float m = v; m = fmaxf(m, dppf<0xB1>(m)); m = fmaxf(m, dppf<0x4E>(m)); m = fmaxf(m, dppf<0x141>(m)); m = fmaxf(m, dppf<0x140>(m));
	s_nop 1
	v_max_f32_dpp v149, v149, v149 quad_perm:[2,3,0,1] row_mask:0xf bank_mask:0xf bound_ctrl:1


; template <int CTRL> __device__ __forceinline__ float dppf(float x) { return __builtin_bit_cast(float, __builtin_amdgcn_update_dpp(0, __builtin_bit_cast(int, x), CTRL, 0xF, 0xF, true)); }
; __device__ __forceinline__ void p9_fused4(Frame& F) {
;     ...
;                 float m = v; m = fmaxf(m, dppf<0xB1>(m)); m = fmaxf(m, dppf<0x4E>(m)); m = fmaxf(m, dppf<0x141>(m)); m = fmaxf(m, dppf<0x140>(m));
	s_nop 1
	v_max_f32_dpp v149, v149, v149 row_half_mirror row_mask:0xf bank_mask:0xf bound_ctrl:1


; template <int CTRL> __device__ __forceinline__ float dppf(float x) { return __builtin_bit_cast(float, __builtin_amdgcn_update_dpp(0, __builtin_bit_cast(int, x), CTRL, 0xF, 0xF, true)); }
; __device__ __forceinline__ void p9_fused4(Frame& F) {
;     ...
;                 float m = v; m = fmaxf(m, dppf<0xB1>(m)); m = fmaxf(m, dppf<0x4E>(m)); m = fmaxf(m, dppf<0x141>(m)); m = fmaxf(m, dppf<0x140>(m));
	s_nop 1
	v_max_f32_dpp v149, v149, v149 row_mirror row_mask:0xf bank_mask:0xf bound_ctrl:1


; template <int CTRL> __device__ __forceinline__ float dppf(float x) { return __builtin_bit_cast(float, __builtin_amdgcn_update_dpp(0, __builtin_bit_cast(int, x), CTRL, 0xF, 0xF, true)); }
; __device__ __forceinline__ void p9_fused4(Frame& F) {
;     ...
;                 float m = v; m = fmaxf(m, dppf<0xB1>(m)); m = fmaxf(m, dppf<0x4E>(m)); m = fmaxf(m, dppf<0x141>(m)); m = fmaxf(m, dppf<0x140>(m));
;                 const float r0 = __builtin_bit_cast(float, __builtin_amdgcn_readlane(__builtin_bit_cast(int, m), 0)), r1 = __builtin_bit_cast(float, __builtin_amdgcn_readlane(__builtin_bit_cast(int, m), 16));
;                 const float r2 = __builtin_bit_cast(float, __builtin_amdgcn_readlane(__builtin_bit_cast(int, m), 32)), r3 = __builtin_bit_cast(float, __builtin_amdgcn_readlane(__builtin_bit_cast(int, m), 48));
;                 const float wm = fmaxf(fmaxf(r0, r1), fmaxf(r2, r3));
;                 const unsigned long long bal = __builtin_amdgcn_ballot_w64(v == wm);
;                 const int selL = (int)__builtin_ctzll(bal);
;                 ssum += __builtin_bit_cast(float, __builtin_amdgcn_readlane(__builtin_bit_cast(int, score), selL));
;                 if (lane == selL) { r = kk; v = -__builtin_inff(); }
	s_nop 0
	v_readlane_b32 s60, v149, 32
	v_readlane_b32 s61, v149, 48
	v_readlane_b32 s22, v149, 0
	v_readlane_b32 s23, v149, 16
	v_max_f32_e64 v149, s61, s61
	v_max_f32_e64 v150, s60, s60
	v_max_f32_e32 v149, v150, v149
	v_mov_b32_e32 v150, s23
	v_max3_f32 v149, s22, v150, v149
	v_cmp_eq_f32_e32 vcc, v147, v149
	s_ff1_i32_b64 s22, vcc
	v_cmp_eq_u32_e32 vcc, s22, v163
	v_readlane_b32 s60, v146, s22
	s_nop 0
	v_cndmask_b32_e32 v147, v147, v211, vcc
	v_max_f32_e32 v150, v147, v147
	v_cndmask_b32_e64 v148, v148, 4, vcc
	v_max_f32_dpp v149, v147, v150 quad_perm:[1,0,3,2] row_mask:0xf bank_mask:0xf bound_ctrl:1


; template <int CTRL> __device__ __forceinline__ float dppf(float x) { return __builtin_bit_cast(float, __builtin_amdgcn_update_dpp(0, __builtin_bit_cast(int, x), CTRL, 0xF, 0xF, true)); }
; __device__ __forceinline__ void p9_fused4(Frame& F) {
;     ...
;                 float m = v; m = fmaxf(m, dppf<0xB1>(m)); m = fmaxf(m, dppf<0x4E>(m)); m = fmaxf(m, dppf<0x141>(m)); m = fmaxf(m, dppf<0x140>(m));
	s_nop 1
	v_max_f32_dpp v149, v149, v149 quad_perm:[2,3,0,1] row_mask:0xf bank_mask:0xf bound_ctrl:1


; template <int CTRL> __device__ __forceinline__ float dppf(float x) { return __builtin_bit_cast(float, __builtin_amdgcn_update_dpp(0, __builtin_bit_cast(int, x), CTRL, 0xF, 0xF, true)); }
; __device__ __forceinline__ void p9_fused4(Frame& F) {
;     ...
;                 float m = v; m = fmaxf(m, dppf<0xB1>(m)); m = fmaxf(m, dppf<0x4E>(m)); m = fmaxf(m, dppf<0x141>(m)); m = fmaxf(m, dppf<0x140>(m));
	s_nop 1
	v_max_f32_dpp v149, v149, v149 row_half_mirror row_mask:0xf bank_mask:0xf bound_ctrl:1


; template <int CTRL> __device__ __forceinline__ float dppf(float x) { return __builtin_bit_cast(float, __builtin_amdgcn_update_dpp(0, __builtin_bit_cast(int, x), CTRL, 0xF, 0xF, true)); }
; __device__ __forceinline__ void p9_fused4(Frame& F) {
;     ...
;                 float m = v; m = fmaxf(m, dppf<0xB1>(m)); m = fmaxf(m, dppf<0x4E>(m)); m = fmaxf(m, dppf<0x141>(m)); m = fmaxf(m, dppf<0x140>(m));
	s_nop 1
	v_max_f32_dpp v149, v149, v149 row_mirror row_mask:0xf bank_mask:0xf bound_ctrl:1


; template <int CTRL> __device__ __forceinline__ float dppf(float x) { return __builtin_bit_cast(float, __builtin_amdgcn_update_dpp(0, __builtin_bit_cast(int, x), CTRL, 0xF, 0xF, true)); }
; __device__ __forceinline__ void p9_fused4(Frame& F) {
;     ...
;                 float m = v; m = fmaxf(m, dppf<0xB1>(m)); m = fmaxf(m, dppf<0x4E>(m)); m = fmaxf(m, dppf<0x141>(m)); m = fmaxf(m, dppf<0x140>(m));
;                 const float r0 = __builtin_bit_cast(float, __builtin_amdgcn_readlane(__builtin_bit_cast(int, m), 0)), r1 = __builtin_bit_cast(float, __builtin_amdgcn_readlane(__builtin_bit_cast(int, m), 16));
;                 const float r2 = __builtin_bit_cast(float, __builtin_amdgcn_readlane(__builtin_bit_cast(int, m), 32)), r3 = __builtin_bit_cast(float, __builtin_amdgcn_readlane(__builtin_bit_cast(int, m), 48));
;                 const float wm = fmaxf(fmaxf(r0, r1), fmaxf(r2, r3));
;                 const unsigned long long bal = __builtin_amdgcn_ballot_w64(v == wm);
;                 const int selL = (int)__builtin_ctzll(bal);
;                 ssum += __builtin_bit_cast(float, __builtin_amdgcn_readlane(__builtin_bit_cast(int, score), selL));
;                 if (lane == selL) { r = kk; v = -__builtin_inff(); }
	s_nop 0
	v_readlane_b32 s61, v149, 32
	v_readlane_b32 s62, v149, 48
	v_readlane_b32 s22, v149, 0
	v_readlane_b32 s23, v149, 16
	v_max_f32_e64 v149, s62, s62
	v_max_f32_e64 v150, s61, s61
	v_max_f32_e32 v149, v150, v149
	v_mov_b32_e32 v150, s23
	v_max3_f32 v149, s22, v150, v149
	v_cmp_eq_f32_e32 vcc, v147, v149
	s_ff1_i32_b64 s22, vcc
	v_cmp_eq_u32_e32 vcc, s22, v163
	v_readlane_b32 s61, v146, s22
	s_nop 0
	v_cndmask_b32_e32 v147, v147, v211, vcc
	v_max_f32_e32 v150, v147, v147
	v_cndmask_b32_e64 v148, v148, 5, vcc
	v_max_f32_dpp v149, v147, v150 quad_perm:[1,0,3,2] row_mask:0xf bank_mask:0xf bound_ctrl:1


; template <int CTRL> __device__ __forceinline__ float dppf(float x) { return __builtin_bit_cast(float, __builtin_amdgcn_update_dpp(0, __builtin_bit_cast(int, x), CTRL, 0xF, 0xF, true)); }
; __device__ __forceinline__ void p9_fused4(Frame& F) {
;     ...
;                 float m = v; m = fmaxf(m, dppf<0xB1>(m)); m = fmaxf(m, dppf<0x4E>(m)); m = fmaxf(m, dppf<0x141>(m)); m = fmaxf(m, dppf<0x140>(m));
	s_nop 1
	v_max_f32_dpp v149, v149, v149 quad_perm:[2,3,0,1] row_mask:0xf bank_mask:0xf bound_ctrl:1


; template <int CTRL> __device__ __forceinline__ float dppf(float x) { return __builtin_bit_cast(float, __builtin_amdgcn_update_dpp(0, __builtin_bit_cast(int, x), CTRL, 0xF, 0xF, true)); }
; __device__ __forceinline__ void p9_fused4(Frame& F) {
;     ...
;                 float m = v; m = fmaxf(m, dppf<0xB1>(m)); m = fmaxf(m, dppf<0x4E>(m)); m = fmaxf(m, dppf<0x141>(m)); m = fmaxf(m, dppf<0x140>(m));
	s_nop 1
	v_max_f32_dpp v149, v149, v149 row_half_mirror row_mask:0xf bank_mask:0xf bound_ctrl:1


; template <int CTRL> __device__ __forceinline__ float dppf(float x) { return __builtin_bit_cast(float, __builtin_amdgcn_update_dpp(0, __builtin_bit_cast(int, x), CTRL, 0xF, 0xF, true)); }
; __device__ __forceinline__ void p9_fused4(Frame& F) {
;     ...
;                 float m = v; m = fmaxf(m, dppf<0xB1>(m)); m = fmaxf(m, dppf<0x4E>(m)); m = fmaxf(m, dppf<0x141>(m)); m = fmaxf(m, dppf<0x140>(m));
	s_nop 1
	v_max_f32_dpp v149, v149, v149 row_mirror row_mask:0xf bank_mask:0xf bound_ctrl:1


; template <int CTRL> __device__ __forceinline__ float dppf(float x) { return __builtin_bit_cast(float, __builtin_amdgcn_update_dpp(0, __builtin_bit_cast(int, x), CTRL, 0xF, 0xF, true)); }
; __device__ __forceinline__ void p9_fused4(Frame& F) {
;     ...
;                 float m = v; m = fmaxf(m, dppf<0xB1>(m)); m = fmaxf(m, dppf<0x4E>(m)); m = fmaxf(m, dppf<0x141>(m)); m = fmaxf(m, dppf<0x140>(m));
;                 const float r0 = __builtin_bit_cast(float, __builtin_amdgcn_readlane(__builtin_bit_cast(int, m), 0)), r1 = __builtin_bit_cast(float, __builtin_amdgcn_readlane(__builtin_bit_cast(int, m), 16));
;                 const float r2 = __builtin_bit_cast(float, __builtin_amdgcn_readlane(__builtin_bit_cast(int, m), 32)), r3 = __builtin_bit_cast(float, __builtin_amdgcn_readlane(__builtin_bit_cast(int, m), 48));
;                 const float wm = fmaxf(fmaxf(r0, r1), fmaxf(r2, r3));
;                 const unsigned long long bal = __builtin_amdgcn_ballot_w64(v == wm);
;                 const int selL = (int)__builtin_ctzll(bal);
;                 ssum += __builtin_bit_cast(float, __builtin_amdgcn_readlane(__builtin_bit_cast(int, score), selL));
;                 if (lane == selL) { r = kk; v = -__builtin_inff(); }
	s_nop 0
	v_readlane_b32 s62, v149, 32
	v_readlane_b32 s63, v149, 48
	v_readlane_b32 s22, v149, 0
	v_readlane_b32 s23, v149, 16
	v_max_f32_e64 v149, s63, s63
	v_max_f32_e64 v150, s62, s62
	v_max_f32_e32 v149, v150, v149
	v_mov_b32_e32 v150, s23
	v_max3_f32 v149, s22, v150, v149
	v_cmp_eq_f32_e32 vcc, v147, v149
	s_ff1_i32_b64 s22, vcc
	v_cmp_eq_u32_e32 vcc, s22, v163
	v_readlane_b32 s62, v146, s22
	s_nop 0
	v_cndmask_b32_e32 v147, v147, v211, vcc
	v_max_f32_e32 v150, v147, v147
	v_cndmask_b32_e64 v148, v148, 6, vcc
	v_max_f32_dpp v149, v147, v150 quad_perm:[1,0,3,2] row_mask:0xf bank_mask:0xf bound_ctrl:1


; template <int CTRL> __device__ __forceinline__ float dppf(float x) { return __builtin_bit_cast(float, __builtin_amdgcn_update_dpp(0, __builtin_bit_cast(int, x), CTRL, 0xF, 0xF, true)); }
; __device__ __forceinline__ void p9_fused4(Frame& F) {
;     ...
;                 float m = v; m = fmaxf(m, dppf<0xB1>(m)); m = fmaxf(m, dppf<0x4E>(m)); m = fmaxf(m, dppf<0x141>(m)); m = fmaxf(m, dppf<0x140>(m));
	s_nop 1
	v_max_f32_dpp v149, v149, v149 quad_perm:[2,3,0,1] row_mask:0xf bank_mask:0xf bound_ctrl:1


; template <int CTRL> __device__ __forceinline__ float dppf(float x) { return __builtin_bit_cast(float, __builtin_amdgcn_update_dpp(0, __builtin_bit_cast(int, x), CTRL, 0xF, 0xF, true)); }
; __device__ __forceinline__ void p9_fused4(Frame& F) {
;     ...
;                 float m = v; m = fmaxf(m, dppf<0xB1>(m)); m = fmaxf(m, dppf<0x4E>(m)); m = fmaxf(m, dppf<0x141>(m)); m = fmaxf(m, dppf<0x140>(m));
	s_nop 1
	v_max_f32_dpp v149, v149, v149 row_half_mirror row_mask:0xf bank_mask:0xf bound_ctrl:1


; template <int CTRL> __device__ __forceinline__ float dppf(float x) { return __builtin_bit_cast(float, __builtin_amdgcn_update_dpp(0, __builtin_bit_cast(int, x), CTRL, 0xF, 0xF, true)); }
; __device__ __forceinline__ void p9_fused4(Frame& F) {
;     ...
;                 float m = v; m = fmaxf(m, dppf<0xB1>(m)); m = fmaxf(m, dppf<0x4E>(m)); m = fmaxf(m, dppf<0x141>(m)); m = fmaxf(m, dppf<0x140>(m));
	s_nop 1
	v_max_f32_dpp v149, v149, v149 row_mirror row_mask:0xf bank_mask:0xf bound_ctrl:1


; template <int CTRL> __device__ __forceinline__ float dppf(float x) { return __builtin_bit_cast(float, __builtin_amdgcn_update_dpp(0, __builtin_bit_cast(int, x), CTRL, 0xF, 0xF, true)); }
; __device__ __forceinline__ void p9_fused4(Frame& F) {
;     ...
;             const float logit = lg[tl * 64 + lane];
;             const float score = 1.f / (1.f + __expf(-logit)), choice = score + rb;
;             float m1 = choice; m1 = fmaxf(m1, dppf<0xB1>(m1)); m1 = fmaxf(m1, dppf<0x4E>(m1)); m1 = fmaxf(m1, dppf<0x141>(m1));
;     ...
;                 const int selL = (int)__builtin_ctzll(bal);
;                 ssum += __builtin_bit_cast(float, __builtin_amdgcn_readlane(__builtin_bit_cast(int, score), selL));
;                 if (lane == selL) { r = kk; v = -__builtin_inff(); }
;             }
;             const bool sel = r < 8;
;             if (sel) { WSP(int, WS_EIDX)[(size_t)t * 8 + r] = lane; WSP(float, WS_EW)[(size_t)t * 8 + r] = score / ssum * 2.5f; if (rp_ == 0) atomicAdd((int*)&hist[lane], 1); }
	s_nop 0
	v_readlane_b32 s63, v149, 32
	v_readlane_b32 s64, v149, 48
	v_readlane_b32 s22, v149, 0
	v_readlane_b32 s23, v149, 16
	v_max_f32_e64 v149, s64, s64
	v_max_f32_e64 v150, s63, s63
	v_max_f32_e32 v149, v150, v149
	v_mov_b32_e32 v150, s23
	v_max3_f32 v149, s22, v150, v149
	v_cmp_eq_f32_e32 vcc, v147, v149
	s_ff1_i32_b64 s22, vcc
	v_cmp_ne_u32_e32 vcc, s22, v163
	v_readlane_b32 s63, v146, s22
	s_nop 0
	v_cndmask_b32_e32 v164, 7, v148, vcc
	v_cmp_gt_u32_e32 vcc, 8, v164
	s_and_saveexec_b64 s[22:23], vcc
	s_cbranch_execz .LBB0_1407
	v_add_f32_e64 v147, s56, 0
	v_add_f32_e32 v147, s57, v147
	v_add_f32_e32 v147, s58, v147
	v_add_f32_e32 v147, s59, v147
	v_add_f32_e32 v147, s60, v147
	v_add_f32_e32 v147, s61, v147
	v_add_f32_e32 v147, s62, v147
	v_add_f32_e32 v147, s63, v147
	v_div_scale_f32 v152, s[56:57], v147, v147, v146
	v_rcp_f32_e32 v153, v152
	s_lshl_b64 s[24:25], s[24:25], 5
	v_lshlrev_b64 v[148:149], 2, v[164:165]
	v_or_b32_e32 v149, s25, v149
	v_or_b32_e32 v148, s24, v148
	v_lshl_add_u64 v[150:151], s[46:47], 0, v[148:149]
	global_store_dword v[150:151], v163, off
	v_fma_f32 v150, -v152, v153, 1.0
	v_fmac_f32_e32 v153, v150, v153
	v_div_scale_f32 v150, vcc, v146, v147, v146
	v_mul_f32_e32 v151, v150, v153
	v_fma_f32 v154, -v152, v151, v150
	v_fmac_f32_e32 v151, v154, v153
	v_fma_f32 v150, -v152, v151, v150
	v_div_fmas_f32 v150, v150, v153, v151
	v_div_fixup_f32 v146, v150, v147, v146
	v_mul_f32_e32 v150, 0x40200000, v146
	v_lshl_add_u64 v[146:147], s[48:49], 0, v[148:149]
	global_store_dword v[146:147], v150, off
	ds_add_u32 v193, v209
.LBB0_1407:
	s_or_b64 exec, exec, s[22:23]
	v_add_u32_e32 v146, s41, v191
	ds_read_b32 v146, v146
	s_waitcnt lgkmcnt(0)
	v_mul_f32_e32 v146, 0xbfb8aa3b, v146
	v_exp_f32_e32 v146, v146
	s_nop 0
	v_add_f32_e32 v146, 1.0, v146
	v_div_scale_f32 v147, s[22:23], v146, v146, 1.0
	v_rcp_f32_e32 v148, v147
	v_div_scale_f32 v149, vcc, 1.0, v146, 1.0
	v_fma_f32 v150, -v147, v148, 1.0
	v_fmac_f32_e32 v148, v150, v148
	v_mul_f32_e32 v150, v149, v148
	v_fma_f32 v151, -v147, v150, v149
	v_fmac_f32_e32 v150, v151, v148
	v_fma_f32 v147, -v147, v150, v149
	v_div_fmas_f32 v147, v147, v148, v150
	v_div_fixup_f32 v146, v147, v146, 1.0
	v_add_f32_e32 v147, v182, v146
	s_nop 1
	v_max_f32_dpp v148, v147, v147 quad_perm:[1,0,3,2] row_mask:0xf bank_mask:0xf bound_ctrl:1


; template <int CTRL> __device__ __forceinline__ float dppf(float x) { return __builtin_bit_cast(float, __builtin_amdgcn_update_dpp(0, __builtin_bit_cast(int, x), CTRL, 0xF, 0xF, true)); }
; __device__ __forceinline__ void p9_fused4(Frame& F) {
;     ...
;             float m1 = choice; m1 = fmaxf(m1, dppf<0xB1>(m1)); m1 = fmaxf(m1, dppf<0x4E>(m1)); m1 = fmaxf(m1, dppf<0x141>(m1));
	s_nop 1
	v_max_f32_dpp v148, v148, v148 quad_perm:[2,3,0,1] row_mask:0xf bank_mask:0xf bound_ctrl:1


; template <int CTRL> __device__ __forceinline__ float dppf(float x) { return __builtin_bit_cast(float, __builtin_amdgcn_update_dpp(0, __builtin_bit_cast(int, x), CTRL, 0xF, 0xF, true)); }
; __device__ __forceinline__ void p9_fused4(Frame& F) {
;     ...
;             float m1 = choice; m1 = fmaxf(m1, dppf<0xB1>(m1)); m1 = fmaxf(m1, dppf<0x4E>(m1)); m1 = fmaxf(m1, dppf<0x141>(m1));
	s_nop 1
	v_max_f32_dpp v148, v148, v148 row_half_mirror row_mask:0xf bank_mask:0xf bound_ctrl:1


; template <int CTRL> __device__ __forceinline__ float dppf(float x) { return __builtin_bit_cast(float, __builtin_amdgcn_update_dpp(0, __builtin_bit_cast(int, x), CTRL, 0xF, 0xF, true)); }
; template <int CTRL> __device__ __forceinline__ int dppi(int x) { return __builtin_amdgcn_update_dpp(0, x, CTRL, 0xF, 0xF, true); }
; __device__ __forceinline__ void p9_fused4(Frame& F) {
;     ...
;             int cand = (choice == m1) ? (lane & 7) : 8; cand = min(cand, dppi<0xB1>(cand)); cand = min(cand, dppi<0x4E>(cand)); cand = min(cand, dppi<0x141>(cand));
;             float m2 = ((lane & 7) == cand) ? -__builtin_inff() : choice; m2 = fmaxf(m2, dppf<0xB1>(m2)); m2 = fmaxf(m2, dppf<0x4E>(m2)); m2 = fmaxf(m2, dppf<0x141>(m2));
	v_cmp_eq_f32_e32 vcc, v147, v148
	s_nop 1
	v_cndmask_b32_e32 v149, 8, v192, vcc
	s_nop 1
	v_min_i32_dpp v149, v149, v149 quad_perm:[1,0,3,2] row_mask:0xf bank_mask:0xf bound_ctrl:1
	s_nop 1
	v_min_i32_dpp v149, v149, v149 quad_perm:[2,3,0,1] row_mask:0xf bank_mask:0xf bound_ctrl:1
	s_nop 1
	v_min_i32_dpp v149, v149, v149 row_half_mirror row_mask:0xf bank_mask:0xf bound_ctrl:1
	v_cmp_ne_u32_e32 vcc, v192, v149
	s_nop 1
	v_cndmask_b32_e32 v149, v211, v147, vcc
	s_nop 1
	v_max_f32_dpp v149, v149, v149 quad_perm:[1,0,3,2] row_mask:0xf bank_mask:0xf bound_ctrl:1


; template <int CTRL> __device__ __forceinline__ float dppf(float x) { return __builtin_bit_cast(float, __builtin_amdgcn_update_dpp(0, __builtin_bit_cast(int, x), CTRL, 0xF, 0xF, true)); }
; __device__ __forceinline__ void p9_fused4(Frame& F) {
;     ...
;             float m2 = ((lane & 7) == cand) ? -__builtin_inff() : choice; m2 = fmaxf(m2, dppf<0xB1>(m2)); m2 = fmaxf(m2, dppf<0x4E>(m2)); m2 = fmaxf(m2, dppf<0x141>(m2));
	s_nop 1
	v_max_f32_dpp v149, v149, v149 quad_perm:[2,3,0,1] row_mask:0xf bank_mask:0xf bound_ctrl:1


; template <int CTRL> __device__ __forceinline__ float dppf(float x) { return __builtin_bit_cast(float, __builtin_amdgcn_update_dpp(0, __builtin_bit_cast(int, x), CTRL, 0xF, 0xF, true)); }
; __device__ __forceinline__ void p9_fused4(Frame& F) {
;     ...
;             float m2 = ((lane & 7) == cand) ? -__builtin_inff() : choice; m2 = fmaxf(m2, dppf<0xB1>(m2)); m2 = fmaxf(m2, dppf<0x4E>(m2)); m2 = fmaxf(m2, dppf<0x141>(m2));
	s_nop 1
	v_max_f32_dpp v149, v149, v149 row_half_mirror row_mask:0xf bank_mask:0xf bound_ctrl:1


; template <int CTRL> __device__ __forceinline__ float dppf(float x) { return __builtin_bit_cast(float, __builtin_amdgcn_update_dpp(0, __builtin_bit_cast(int, x), CTRL, 0xF, 0xF, true)); }
; __device__ __forceinline__ void p9_fused4(Frame& F) {
;     ...
;             const float gs = m1 + m2; const int g = lane >> 3; int rank = 0;
; #pragma unroll
;             for (int gg = 0; gg < 8; ++gg) { const float sgg = __builtin_bit_cast(float, __builtin_amdgcn_readlane(__builtin_bit_cast(int, gs), gg * 8)); rank += (sgg > gs || (sgg == gs && gg < g)) ? 1 : 0; }
;             const float masked = (rank < 4) ? choice : -1e30f;
;             float v = masked, ssum = 0.f; int r = 8;
; #pragma unroll
;             for (int kk = 0; kk < 8; ++kk) {
;                 float m = v; m = fmaxf(m, dppf<0xB1>(m)); m = fmaxf(m, dppf<0x4E>(m)); m = fmaxf(m, dppf<0x141>(m)); m = fmaxf(m, dppf<0x140>(m));
	v_add_f32_e32 v148, v148, v149
	s_nop 0
	v_readlane_b32 s22, v148, 0
	v_readlane_b32 s56, v148, 8
	s_nop 0
	v_cmp_gt_f32_e32 vcc, s22, v148
	v_cmp_eq_f32_e64 s[22:23], s22, v148
	s_and_b64 s[22:23], s[22:23], s[6:7]
	s_or_b64 s[22:23], vcc, s[22:23]
	v_cmp_eq_f32_e32 vcc, s56, v148
	v_cmp_gt_f32_e64 s[24:25], s56, v148
	v_cndmask_b32_e64 v149, 0, 1, s[22:23]
	s_and_b64 s[22:23], vcc, s[8:9]
	s_or_b64 s[22:23], s[24:25], s[22:23]
	v_cndmask_b32_e64 v150, 0, 1, s[22:23]
	v_readlane_b32 s22, v148, 16
	s_nop 1
	v_cmp_gt_f32_e32 vcc, s22, v148
	v_cmp_eq_f32_e64 s[22:23], s22, v148
	s_and_b64 s[22:23], s[22:23], s[10:11]
	s_or_b64 s[22:23], vcc, s[22:23]
	v_cndmask_b32_e64 v151, 0, 1, s[22:23]
	v_readlane_b32 s22, v148, 24
	s_nop 1
	v_cmp_gt_f32_e32 vcc, s22, v148
	v_cmp_eq_f32_e64 s[22:23], s22, v148
	s_and_b64 s[22:23], s[22:23], s[12:13]
	s_or_b64 s[22:23], vcc, s[22:23]
	v_cndmask_b32_e64 v152, 0, 1, s[22:23]
	v_readlane_b32 s22, v148, 32
	s_nop 1
	v_cmp_gt_f32_e32 vcc, s22, v148
	v_cmp_eq_f32_e64 s[22:23], s22, v148
	s_and_b64 s[22:23], s[22:23], s[14:15]
	s_or_b64 s[22:23], vcc, s[22:23]
	v_cndmask_b32_e64 v153, 0, 1, s[22:23]
	v_readlane_b32 s22, v148, 40
	s_nop 1
	v_cmp_gt_f32_e32 vcc, s22, v148
	v_cmp_eq_f32_e64 s[22:23], s22, v148
	s_and_b64 s[22:23], s[22:23], s[16:17]
	s_or_b64 s[22:23], vcc, s[22:23]
	v_cndmask_b32_e64 v154, 0, 1, s[22:23]
	v_readlane_b32 s22, v148, 48
	s_nop 1
	v_cmp_gt_f32_e32 vcc, s22, v148
	v_cmp_eq_f32_e64 s[22:23], s22, v148
	s_and_b64 s[22:23], s[18:19], s[22:23]
	s_or_b64 s[22:23], vcc, s[22:23]
	v_cndmask_b32_e64 v155, 0, 1, s[22:23]
	v_readlane_b32 s22, v148, 56
	s_nop 1
	v_cmp_gt_f32_e32 vcc, s22, v148
	s_nop 1
	v_cndmask_b32_e64 v148, 0, 1, vcc
	v_add_u32_e32 v148, v150, v148
	v_add3_u32 v148, v148, v149, v151
	v_add3_u32 v148, v148, v152, v153
	v_add3_u32 v148, v148, v154, v155
	v_cmp_gt_u32_e32 vcc, 4, v148
	s_nop 1
	v_cndmask_b32_e32 v147, v212, v147, vcc
	s_nop 1
	v_max_f32_dpp v148, v147, v147 quad_perm:[1,0,3,2] row_mask:0xf bank_mask:0xf bound_ctrl:1


; template <int CTRL> __device__ __forceinline__ float dppf(float x) { return __builtin_bit_cast(float, __builtin_amdgcn_update_dpp(0, __builtin_bit_cast(int, x), CTRL, 0xF, 0xF, true)); }
; __device__ __forceinline__ void p9_fused4(Frame& F) {
;     ...
;                 float m = v; m = fmaxf(m, dppf<0xB1>(m)); m = fmaxf(m, dppf<0x4E>(m)); m = fmaxf(m, dppf<0x141>(m)); m = fmaxf(m, dppf<0x140>(m));
	s_nop 1
	v_max_f32_dpp v148, v148, v148 quad_perm:[2,3,0,1] row_mask:0xf bank_mask:0xf bound_ctrl:1


; template <int CTRL> __device__ __forceinline__ float dppf(float x) { return __builtin_bit_cast(float, __builtin_amdgcn_update_dpp(0, __builtin_bit_cast(int, x), CTRL, 0xF, 0xF, true)); }
; __device__ __forceinline__ void p9_fused4(Frame& F) {
;     ...
;                 float m = v; m = fmaxf(m, dppf<0xB1>(m)); m = fmaxf(m, dppf<0x4E>(m)); m = fmaxf(m, dppf<0x141>(m)); m = fmaxf(m, dppf<0x140>(m));
	s_nop 1
	v_max_f32_dpp v148, v148, v148 row_half_mirror row_mask:0xf bank_mask:0xf bound_ctrl:1


; template <int CTRL> __device__ __forceinline__ float dppf(float x) { return __builtin_bit_cast(float, __builtin_amdgcn_update_dpp(0, __builtin_bit_cast(int, x), CTRL, 0xF, 0xF, true)); }
; __device__ __forceinline__ void p9_fused4(Frame& F) {
;     ...
;                 float m = v; m = fmaxf(m, dppf<0xB1>(m)); m = fmaxf(m, dppf<0x4E>(m)); m = fmaxf(m, dppf<0x141>(m)); m = fmaxf(m, dppf<0x140>(m));
	s_nop 1
	v_max_f32_dpp v148, v148, v148 row_mirror row_mask:0xf bank_mask:0xf bound_ctrl:1


; template <int CTRL> __device__ __forceinline__ float dppf(float x) { return __builtin_bit_cast(float, __builtin_amdgcn_update_dpp(0, __builtin_bit_cast(int, x), CTRL, 0xF, 0xF, true)); }
; __device__ __forceinline__ void p9_fused4(Frame& F) {
;     ...
;                 float m = v; m = fmaxf(m, dppf<0xB1>(m)); m = fmaxf(m, dppf<0x4E>(m)); m = fmaxf(m, dppf<0x141>(m)); m = fmaxf(m, dppf<0x140>(m));
;                 const float r0 = __builtin_bit_cast(float, __builtin_amdgcn_readlane(__builtin_bit_cast(int, m), 0)), r1 = __builtin_bit_cast(float, __builtin_amdgcn_readlane(__builtin_bit_cast(int, m), 16));
;                 const float r2 = __builtin_bit_cast(float, __builtin_amdgcn_readlane(__builtin_bit_cast(int, m), 32)), r3 = __builtin_bit_cast(float, __builtin_amdgcn_readlane(__builtin_bit_cast(int, m), 48));
;                 const float wm = fmaxf(fmaxf(r0, r1), fmaxf(r2, r3));
;                 const unsigned long long bal = __builtin_amdgcn_ballot_w64(v == wm);
;                 const int selL = (int)__builtin_ctzll(bal);
;                 ssum += __builtin_bit_cast(float, __builtin_amdgcn_readlane(__builtin_bit_cast(int, score), selL));
;                 if (lane == selL) { r = kk; v = -__builtin_inff(); }
	s_nop 0
	v_readlane_b32 s24, v148, 32
	v_readlane_b32 s25, v148, 48
	v_readlane_b32 s22, v148, 0
	v_readlane_b32 s23, v148, 16
	v_max_f32_e64 v148, s25, s25
	v_max_f32_e64 v149, s24, s24
	v_max_f32_e32 v148, v149, v148
	v_mov_b32_e32 v149, s23
	v_max3_f32 v148, s22, v149, v148
	v_cmp_eq_f32_e32 vcc, v147, v148
	s_ff1_i32_b64 s22, vcc
	v_cmp_eq_u32_e32 vcc, s22, v163
	v_readlane_b32 s24, v146, s22
	s_nop 0
	v_cndmask_b32_e32 v147, v147, v211, vcc
	v_cndmask_b32_e64 v148, 8, 0, vcc
	s_nop 0
	v_max_f32_dpp v149, v147, v147 quad_perm:[1,0,3,2] row_mask:0xf bank_mask:0xf bound_ctrl:1


; template <int CTRL> __device__ __forceinline__ float dppf(float x) { return __builtin_bit_cast(float, __builtin_amdgcn_update_dpp(0, __builtin_bit_cast(int, x), CTRL, 0xF, 0xF, true)); }
; __device__ __forceinline__ void p9_fused4(Frame& F) {
;     ...
;                 float m = v; m = fmaxf(m, dppf<0xB1>(m)); m = fmaxf(m, dppf<0x4E>(m)); m = fmaxf(m, dppf<0x141>(m)); m = fmaxf(m, dppf<0x140>(m));
	s_nop 1
	v_max_f32_dpp v149, v149, v149 quad_perm:[2,3,0,1] row_mask:0xf bank_mask:0xf bound_ctrl:1


; template <int CTRL> __device__ __forceinline__ float dppf(float x) { return __builtin_bit_cast(float, __builtin_amdgcn_update_dpp(0, __builtin_bit_cast(int, x), CTRL, 0xF, 0xF, true)); }
; __device__ __forceinline__ void p9_fused4(Frame& F) {
;     ...
;                 float m = v; m = fmaxf(m, dppf<0xB1>(m)); m = fmaxf(m, dppf<0x4E>(m)); m = fmaxf(m, dppf<0x141>(m)); m = fmaxf(m, dppf<0x140>(m));
	s_nop 1
	v_max_f32_dpp v149, v149, v149 row_half_mirror row_mask:0xf bank_mask:0xf bound_ctrl:1


; template <int CTRL> __device__ __forceinline__ float dppf(float x) { return __builtin_bit_cast(float, __builtin_amdgcn_update_dpp(0, __builtin_bit_cast(int, x), CTRL, 0xF, 0xF, true)); }
; __device__ __forceinline__ void p9_fused4(Frame& F) {
;     ...
;                 float m = v; m = fmaxf(m, dppf<0xB1>(m)); m = fmaxf(m, dppf<0x4E>(m)); m = fmaxf(m, dppf<0x141>(m)); m = fmaxf(m, dppf<0x140>(m));
	s_nop 1
	v_max_f32_dpp v149, v149, v149 row_mirror row_mask:0xf bank_mask:0xf bound_ctrl:1


; template <int CTRL> __device__ __forceinline__ float dppf(float x) { return __builtin_bit_cast(float, __builtin_amdgcn_update_dpp(0, __builtin_bit_cast(int, x), CTRL, 0xF, 0xF, true)); }
; __device__ __forceinline__ void p9_fused4(Frame& F) {
;     ...
;                 float m = v; m = fmaxf(m, dppf<0xB1>(m)); m = fmaxf(m, dppf<0x4E>(m)); m = fmaxf(m, dppf<0x141>(m)); m = fmaxf(m, dppf<0x140>(m));
;                 const float r0 = __builtin_bit_cast(float, __builtin_amdgcn_readlane(__builtin_bit_cast(int, m), 0)), r1 = __builtin_bit_cast(float, __builtin_amdgcn_readlane(__builtin_bit_cast(int, m), 16));
;                 const float r2 = __builtin_bit_cast(float, __builtin_amdgcn_readlane(__builtin_bit_cast(int, m), 32)), r3 = __builtin_bit_cast(float, __builtin_amdgcn_readlane(__builtin_bit_cast(int, m), 48));
;                 const float wm = fmaxf(fmaxf(r0, r1), fmaxf(r2, r3));
;                 const unsigned long long bal = __builtin_amdgcn_ballot_w64(v == wm);
;                 const int selL = (int)__builtin_ctzll(bal);
;                 ssum += __builtin_bit_cast(float, __builtin_amdgcn_readlane(__builtin_bit_cast(int, score), selL));
;                 if (lane == selL) { r = kk; v = -__builtin_inff(); }
	s_nop 0
	v_readlane_b32 s25, v149, 32
	v_readlane_b32 s56, v149, 48
	v_readlane_b32 s22, v149, 0
	v_readlane_b32 s23, v149, 16
	v_max_f32_e64 v149, s56, s56
	v_max_f32_e64 v150, s25, s25
	v_max_f32_e32 v149, v150, v149
	v_mov_b32_e32 v150, s23
	v_max3_f32 v149, s22, v150, v149
	v_cmp_eq_f32_e32 vcc, v147, v149
	s_ff1_i32_b64 s22, vcc
	v_cmp_eq_u32_e32 vcc, s22, v163
	v_readlane_b32 s25, v146, s22
	s_nop 0
	v_cndmask_b32_e32 v147, v147, v211, vcc
	v_cndmask_b32_e64 v148, v148, 1, vcc
	s_nop 0
	v_max_f32_dpp v149, v147, v147 quad_perm:[1,0,3,2] row_mask:0xf bank_mask:0xf bound_ctrl:1


; template <int CTRL> __device__ __forceinline__ float dppf(float x) { return __builtin_bit_cast(float, __builtin_amdgcn_update_dpp(0, __builtin_bit_cast(int, x), CTRL, 0xF, 0xF, true)); }
; __device__ __forceinline__ void p9_fused4(Frame& F) {
;     ...
;                 float m = v; m = fmaxf(m, dppf<0xB1>(m)); m = fmaxf(m, dppf<0x4E>(m)); m = fmaxf(m, dppf<0x141>(m)); m = fmaxf(m, dppf<0x140>(m));
	s_nop 1
	v_max_f32_dpp v149, v149, v149 quad_perm:[2,3,0,1] row_mask:0xf bank_mask:0xf bound_ctrl:1


; template <int CTRL> __device__ __forceinline__ float dppf(float x) { return __builtin_bit_cast(float, __builtin_amdgcn_update_dpp(0, __builtin_bit_cast(int, x), CTRL, 0xF, 0xF, true)); }
; __device__ __forceinline__ void p9_fused4(Frame& F) {
;     ...
;                 float m = v; m = fmaxf(m, dppf<0xB1>(m)); m = fmaxf(m, dppf<0x4E>(m)); m = fmaxf(m, dppf<0x141>(m)); m = fmaxf(m, dppf<0x140>(m));
	s_nop 1
	v_max_f32_dpp v149, v149, v149 row_half_mirror row_mask:0xf bank_mask:0xf bound_ctrl:1


; template <int CTRL> __device__ __forceinline__ float dppf(float x) { return __builtin_bit_cast(float, __builtin_amdgcn_update_dpp(0, __builtin_bit_cast(int, x), CTRL, 0xF, 0xF, true)); }
; __device__ __forceinline__ void p9_fused4(Frame& F) {
;     ...
;                 float m = v; m = fmaxf(m, dppf<0xB1>(m)); m = fmaxf(m, dppf<0x4E>(m)); m = fmaxf(m, dppf<0x141>(m)); m = fmaxf(m, dppf<0x140>(m));
	s_nop 1
	v_max_f32_dpp v149, v149, v149 row_mirror row_mask:0xf bank_mask:0xf bound_ctrl:1


; template <int CTRL> __device__ __forceinline__ float dppf(float x) { return __builtin_bit_cast(float, __builtin_amdgcn_update_dpp(0, __builtin_bit_cast(int, x), CTRL, 0xF, 0xF, true)); }
; __device__ __forceinline__ void p9_fused4(Frame& F) {
;     ...
;                 float m = v; m = fmaxf(m, dppf<0xB1>(m)); m = fmaxf(m, dppf<0x4E>(m)); m = fmaxf(m, dppf<0x141>(m)); m = fmaxf(m, dppf<0x140>(m));
;                 const float r0 = __builtin_bit_cast(float, __builtin_amdgcn_readlane(__builtin_bit_cast(int, m), 0)), r1 = __builtin_bit_cast(float, __builtin_amdgcn_readlane(__builtin_bit_cast(int, m), 16));
;                 const float r2 = __builtin_bit_cast(float, __builtin_amdgcn_readlane(__builtin_bit_cast(int, m), 32)), r3 = __builtin_bit_cast(float, __builtin_amdgcn_readlane(__builtin_bit_cast(int, m), 48));
;                 const float wm = fmaxf(fmaxf(r0, r1), fmaxf(r2, r3));
;                 const unsigned long long bal = __builtin_amdgcn_ballot_w64(v == wm);
;                 const int selL = (int)__builtin_ctzll(bal);
;                 ssum += __builtin_bit_cast(float, __builtin_amdgcn_readlane(__builtin_bit_cast(int, score), selL));
;                 if (lane == selL) { r = kk; v = -__builtin_inff(); }
	s_nop 0
	v_readlane_b32 s56, v149, 32
	v_readlane_b32 s57, v149, 48
	v_readlane_b32 s22, v149, 0
	v_readlane_b32 s23, v149, 16
	v_max_f32_e64 v149, s57, s57
	v_max_f32_e64 v150, s56, s56
	v_max_f32_e32 v149, v150, v149
	v_mov_b32_e32 v150, s23
	v_max3_f32 v149, s22, v150, v149
	v_cmp_eq_f32_e32 vcc, v147, v149
	s_ff1_i32_b64 s22, vcc
	v_cmp_eq_u32_e32 vcc, s22, v163
	v_readlane_b32 s56, v146, s22
	s_nop 0
	v_cndmask_b32_e32 v147, v147, v211, vcc
	v_cndmask_b32_e64 v148, v148, 2, vcc
	s_nop 0
	v_max_f32_dpp v149, v147, v147 quad_perm:[1,0,3,2] row_mask:0xf bank_mask:0xf bound_ctrl:1


; template <int CTRL> __device__ __forceinline__ float dppf(float x) { return __builtin_bit_cast(float, __builtin_amdgcn_update_dpp(0, __builtin_bit_cast(int, x), CTRL, 0xF, 0xF, true)); }
; __device__ __forceinline__ void p9_fused4(Frame& F) {
;     ...
;                 float m = v; m = fmaxf(m, dppf<0xB1>(m)); m = fmaxf(m, dppf<0x4E>(m)); m = fmaxf(m, dppf<0x141>(m)); m = fmaxf(m, dppf<0x140>(m));
	s_nop 1
	v_max_f32_dpp v149, v149, v149 quad_perm:[2,3,0,1] row_mask:0xf bank_mask:0xf bound_ctrl:1


; template <int CTRL> __device__ __forceinline__ float dppf(float x) { return __builtin_bit_cast(float, __builtin_amdgcn_update_dpp(0, __builtin_bit_cast(int, x), CTRL, 0xF, 0xF, true)); }
; __device__ __forceinline__ void p9_fused4(Frame& F) {
;     ...
;                 float m = v; m = fmaxf(m, dppf<0xB1>(m)); m = fmaxf(m, dppf<0x4E>(m)); m = fmaxf(m, dppf<0x141>(m)); m = fmaxf(m, dppf<0x140>(m));
	s_nop 1
	v_max_f32_dpp v149, v149, v149 row_half_mirror row_mask:0xf bank_mask:0xf bound_ctrl:1


; template <int CTRL> __device__ __forceinline__ float dppf(float x) { return __builtin_bit_cast(float, __builtin_amdgcn_update_dpp(0, __builtin_bit_cast(int, x), CTRL, 0xF, 0xF, true)); }
; __device__ __forceinline__ void p9_fused4(Frame& F) {
;     ...
;                 float m = v; m = fmaxf(m, dppf<0xB1>(m)); m = fmaxf(m, dppf<0x4E>(m)); m = fmaxf(m, dppf<0x141>(m)); m = fmaxf(m, dppf<0x140>(m));
	s_nop 1
	v_max_f32_dpp v149, v149, v149 row_mirror row_mask:0xf bank_mask:0xf bound_ctrl:1


; template <int CTRL> __device__ __forceinline__ float dppf(float x) { return __builtin_bit_cast(float, __builtin_amdgcn_update_dpp(0, __builtin_bit_cast(int, x), CTRL, 0xF, 0xF, true)); }
; __device__ __forceinline__ void p9_fused4(Frame& F) {
;     ...
;                 float m = v; m = fmaxf(m, dppf<0xB1>(m)); m = fmaxf(m, dppf<0x4E>(m)); m = fmaxf(m, dppf<0x141>(m)); m = fmaxf(m, dppf<0x140>(m));
;                 const float r0 = __builtin_bit_cast(float, __builtin_amdgcn_readlane(__builtin_bit_cast(int, m), 0)), r1 = __builtin_bit_cast(float, __builtin_amdgcn_readlane(__builtin_bit_cast(int, m), 16));
;                 const float r2 = __builtin_bit_cast(float, __builtin_amdgcn_readlane(__builtin_bit_cast(int, m), 32)), r3 = __builtin_bit_cast(float, __builtin_amdgcn_readlane(__builtin_bit_cast(int, m), 48));
;                 const float wm = fmaxf(fmaxf(r0, r1), fmaxf(r2, r3));
;                 const unsigned long long bal = __builtin_amdgcn_ballot_w64(v == wm);
;                 const int selL = (int)__builtin_ctzll(bal);
;                 ssum += __builtin_bit_cast(float, __builtin_amdgcn_readlane(__builtin_bit_cast(int, score), selL));
;                 if (lane == selL) { r = kk; v = -__builtin_inff(); }
	s_nop 0
	v_readlane_b32 s57, v149, 32
	v_readlane_b32 s58, v149, 48
	v_readlane_b32 s22, v149, 0
	v_readlane_b32 s23, v149, 16
	v_max_f32_e64 v149, s58, s58
	v_max_f32_e64 v150, s57, s57
	v_max_f32_e32 v149, v150, v149
	v_mov_b32_e32 v150, s23
	v_max3_f32 v149, s22, v150, v149
	v_cmp_eq_f32_e32 vcc, v147, v149
	s_ff1_i32_b64 s22, vcc
	v_cmp_eq_u32_e32 vcc, s22, v163
	v_readlane_b32 s57, v146, s22
	s_nop 0
	v_cndmask_b32_e32 v147, v147, v211, vcc
	v_cndmask_b32_e64 v148, v148, 3, vcc
	s_nop 0
	v_max_f32_dpp v149, v147, v147 quad_perm:[1,0,3,2] row_mask:0xf bank_mask:0xf bound_ctrl:1


; template <int CTRL> __device__ __forceinline__ float dppf(float x) { return __builtin_bit_cast(float, __builtin_amdgcn_update_dpp(0, __builtin_bit_cast(int, x), CTRL, 0xF, 0xF, true)); }
; __device__ __forceinline__ void p9_fused4(Frame& F) {
;     ...
;                 float m = v; m = fmaxf(m, dppf<0xB1>(m)); m = fmaxf(m, dppf<0x4E>(m)); m = fmaxf(m, dppf<0x141>(m)); m = fmaxf(m, dppf<0x140>(m));
	s_nop 1
	v_max_f32_dpp v149, v149, v149 quad_perm:[2,3,0,1] row_mask:0xf bank_mask:0xf bound_ctrl:1


; template <int CTRL> __device__ __forceinline__ float dppf(float x) { return __builtin_bit_cast(float, __builtin_amdgcn_update_dpp(0, __builtin_bit_cast(int, x), CTRL, 0xF, 0xF, true)); }
; __device__ __forceinline__ void p9_fused4(Frame& F) {
;     ...
;                 float m = v; m = fmaxf(m, dppf<0xB1>(m)); m = fmaxf(m, dppf<0x4E>(m)); m = fmaxf(m, dppf<0x141>(m)); m = fmaxf(m, dppf<0x140>(m));
	s_nop 1
	v_max_f32_dpp v149, v149, v149 row_half_mirror row_mask:0xf bank_mask:0xf bound_ctrl:1


; template <int CTRL> __device__ __forceinline__ float dppf(float x) { return __builtin_bit_cast(float, __builtin_amdgcn_update_dpp(0, __builtin_bit_cast(int, x), CTRL, 0xF, 0xF, true)); }
; __device__ __forceinline__ void p9_fused4(Frame& F) {
;     ...
;                 float m = v; m = fmaxf(m, dppf<0xB1>(m)); m = fmaxf(m, dppf<0x4E>(m)); m = fmaxf(m, dppf<0x141>(m)); m = fmaxf(m, dppf<0x140>(m));
	s_nop 1
	v_max_f32_dpp v149, v149, v149 row_mirror row_mask:0xf bank_mask:0xf bound_ctrl:1


; template <int CTRL> __device__ __forceinline__ float dppf(float x) { return __builtin_bit_cast(float, __builtin_amdgcn_update_dpp(0, __builtin_bit_cast(int, x), CTRL, 0xF, 0xF, true)); }
; __device__ __forceinline__ void p9_fused4(Frame& F) {
;     ...
;                 float m = v; m = fmaxf(m, dppf<0xB1>(m)); m = fmaxf(m, dppf<0x4E>(m)); m = fmaxf(m, dppf<0x141>(m)); m = fmaxf(m, dppf<0x140>(m));
;                 const float r0 = __builtin_bit_cast(float, __builtin_amdgcn_readlane(__builtin_bit_cast(int, m), 0)), r1 = __builtin_bit_cast(float, __builtin_amdgcn_readlane(__builtin_bit_cast(int, m), 16));
;                 const float r2 = __builtin_bit_cast(float, __builtin_amdgcn_readlane(__builtin_bit_cast(int, m), 32)), r3 = __builtin_bit_cast(float, __builtin_amdgcn_readlane(__builtin_bit_cast(int, m), 48));
;                 const float wm = fmaxf(fmaxf(r0, r1), fmaxf(r2, r3));
;                 const unsigned long long bal = __builtin_amdgcn_ballot_w64(v == wm);
;                 const int selL = (int)__builtin_ctzll(bal);
;                 ssum += __builtin_bit_cast(float, __builtin_amdgcn_readlane(__builtin_bit_cast(int, score), selL));
;                 if (lane == selL) { r = kk; v = -__builtin_inff(); }
	s_nop 0
	v_readlane_b32 s58, v149, 32
	v_readlane_b32 s59, v149, 48
	v_readlane_b32 s22, v149, 0
	v_readlane_b32 s23, v149, 16
	v_max_f32_e64 v149, s59, s59
	v_max_f32_e64 v150, s58, s58
	v_max_f32_e32 v149, v150, v149
	v_mov_b32_e32 v150, s23
	v_max3_f32 v149, s22, v150, v149
	v_cmp_eq_f32_e32 vcc, v147, v149
	s_ff1_i32_b64 s22, vcc
	v_cmp_eq_u32_e32 vcc, s22, v163
	v_readlane_b32 s58, v146, s22
	s_nop 0
	v_cndmask_b32_e32 v147, v147, v211, vcc
	v_max_f32_e32 v150, v147, v147
	v_cndmask_b32_e64 v148, v148, 4, vcc
	v_max_f32_dpp v149, v147, v150 quad_perm:[1,0,3,2] row_mask:0xf bank_mask:0xf bound_ctrl:1


; template <int CTRL> __device__ __forceinline__ float dppf(float x) { return __builtin_bit_cast(float, __builtin_amdgcn_update_dpp(0, __builtin_bit_cast(int, x), CTRL, 0xF, 0xF, true)); }
; __device__ __forceinline__ void p9_fused4(Frame& F) {
;     ...
;                 float m = v; m = fmaxf(m, dppf<0xB1>(m)); m = fmaxf(m, dppf<0x4E>(m)); m = fmaxf(m, dppf<0x141>(m)); m = fmaxf(m, dppf<0x140>(m));
	s_nop 1
	v_max_f32_dpp v149, v149, v149 quad_perm:[2,3,0,1] row_mask:0xf bank_mask:0xf bound_ctrl:1


; template <int CTRL> __device__ __forceinline__ float dppf(float x) { return __builtin_bit_cast(float, __builtin_amdgcn_update_dpp(0, __builtin_bit_cast(int, x), CTRL, 0xF, 0xF, true)); }
; __device__ __forceinline__ void p9_fused4(Frame& F) {
;     ...
;                 float m = v; m = fmaxf(m, dppf<0xB1>(m)); m = fmaxf(m, dppf<0x4E>(m)); m = fmaxf(m, dppf<0x141>(m)); m = fmaxf(m, dppf<0x140>(m));
	s_nop 1
	v_max_f32_dpp v149, v149, v149 row_half_mirror row_mask:0xf bank_mask:0xf bound_ctrl:1


; template <int CTRL> __device__ __forceinline__ float dppf(float x) { return __builtin_bit_cast(float, __builtin_amdgcn_update_dpp(0, __builtin_bit_cast(int, x), CTRL, 0xF, 0xF, true)); }
; __device__ __forceinline__ void p9_fused4(Frame& F) {
;     ...
;                 float m = v; m = fmaxf(m, dppf<0xB1>(m)); m = fmaxf(m, dppf<0x4E>(m)); m = fmaxf(m, dppf<0x141>(m)); m = fmaxf(m, dppf<0x140>(m));
	s_nop 1
	v_max_f32_dpp v149, v149, v149 row_mirror row_mask:0xf bank_mask:0xf bound_ctrl:1


; template <int CTRL> __device__ __forceinline__ float dppf(float x) { return __builtin_bit_cast(float, __builtin_amdgcn_update_dpp(0, __builtin_bit_cast(int, x), CTRL, 0xF, 0xF, true)); }
; __device__ __forceinline__ void p9_fused4(Frame& F) {
;     ...
;                 float m = v; m = fmaxf(m, dppf<0xB1>(m)); m = fmaxf(m, dppf<0x4E>(m)); m = fmaxf(m, dppf<0x141>(m)); m = fmaxf(m, dppf<0x140>(m));
;                 const float r0 = __builtin_bit_cast(float, __builtin_amdgcn_readlane(__builtin_bit_cast(int, m), 0)), r1 = __builtin_bit_cast(float, __builtin_amdgcn_readlane(__builtin_bit_cast(int, m), 16));
;                 const float r2 = __builtin_bit_cast(float, __builtin_amdgcn_readlane(__builtin_bit_cast(int, m), 32)), r3 = __builtin_bit_cast(float, __builtin_amdgcn_readlane(__builtin_bit_cast(int, m), 48));
;                 const float wm = fmaxf(fmaxf(r0, r1), fmaxf(r2, r3));
;                 const unsigned long long bal = __builtin_amdgcn_ballot_w64(v == wm);
;                 const int selL = (int)__builtin_ctzll(bal);
;                 ssum += __builtin_bit_cast(float, __builtin_amdgcn_readlane(__builtin_bit_cast(int, score), selL));
;                 if (lane == selL) { r = kk; v = -__builtin_inff(); }
	s_nop 0
	v_readlane_b32 s59, v149, 32
	v_readlane_b32 s60, v149, 48
	v_readlane_b32 s22, v149, 0
	v_readlane_b32 s23, v149, 16
	v_max_f32_e64 v149, s60, s60
	v_max_f32_e64 v150, s59, s59
	v_max_f32_e32 v149, v150, v149
	v_mov_b32_e32 v150, s23
	v_max3_f32 v149, s22, v150, v149
	v_cmp_eq_f32_e32 vcc, v147, v149
	s_ff1_i32_b64 s22, vcc
	v_cmp_eq_u32_e32 vcc, s22, v163
	v_readlane_b32 s59, v146, s22
	s_nop 0
	v_cndmask_b32_e32 v147, v147, v211, vcc
	v_max_f32_e32 v150, v147, v147
	v_cndmask_b32_e64 v148, v148, 5, vcc
	v_max_f32_dpp v149, v147, v150 quad_perm:[1,0,3,2] row_mask:0xf bank_mask:0xf bound_ctrl:1


; template <int CTRL> __device__ __forceinline__ float dppf(float x) { return __builtin_bit_cast(float, __builtin_amdgcn_update_dpp(0, __builtin_bit_cast(int, x), CTRL, 0xF, 0xF, true)); }
; __device__ __forceinline__ void p9_fused4(Frame& F) {
;     ...
;                 float m = v; m = fmaxf(m, dppf<0xB1>(m)); m = fmaxf(m, dppf<0x4E>(m)); m = fmaxf(m, dppf<0x141>(m)); m = fmaxf(m, dppf<0x140>(m));
	s_nop 1
	v_max_f32_dpp v149, v149, v149 quad_perm:[2,3,0,1] row_mask:0xf bank_mask:0xf bound_ctrl:1


; template <int CTRL> __device__ __forceinline__ float dppf(float x) { return __builtin_bit_cast(float, __builtin_amdgcn_update_dpp(0, __builtin_bit_cast(int, x), CTRL, 0xF, 0xF, true)); }
; __device__ __forceinline__ void p9_fused4(Frame& F) {
;     ...
;                 float m = v; m = fmaxf(m, dppf<0xB1>(m)); m = fmaxf(m, dppf<0x4E>(m)); m = fmaxf(m, dppf<0x141>(m)); m = fmaxf(m, dppf<0x140>(m));
	s_nop 1
	v_max_f32_dpp v149, v149, v149 row_half_mirror row_mask:0xf bank_mask:0xf bound_ctrl:1


; template <int CTRL> __device__ __forceinline__ float dppf(float x) { return __builtin_bit_cast(float, __builtin_amdgcn_update_dpp(0, __builtin_bit_cast(int, x), CTRL, 0xF, 0xF, true)); }
; __device__ __forceinline__ void p9_fused4(Frame& F) {
;     ...
;                 float m = v; m = fmaxf(m, dppf<0xB1>(m)); m = fmaxf(m, dppf<0x4E>(m)); m = fmaxf(m, dppf<0x141>(m)); m = fmaxf(m, dppf<0x140>(m));
	s_nop 1
	v_max_f32_dpp v149, v149, v149 row_mirror row_mask:0xf bank_mask:0xf bound_ctrl:1


; template <int CTRL> __device__ __forceinline__ float dppf(float x) { return __builtin_bit_cast(float, __builtin_amdgcn_update_dpp(0, __builtin_bit_cast(int, x), CTRL, 0xF, 0xF, true)); }
; __device__ __forceinline__ void p9_fused4(Frame& F) {
;     ...
;                 float m = v; m = fmaxf(m, dppf<0xB1>(m)); m = fmaxf(m, dppf<0x4E>(m)); m = fmaxf(m, dppf<0x141>(m)); m = fmaxf(m, dppf<0x140>(m));
;                 const float r0 = __builtin_bit_cast(float, __builtin_amdgcn_readlane(__builtin_bit_cast(int, m), 0)), r1 = __builtin_bit_cast(float, __builtin_amdgcn_readlane(__builtin_bit_cast(int, m), 16));
;                 const float r2 = __builtin_bit_cast(float, __builtin_amdgcn_readlane(__builtin_bit_cast(int, m), 32)), r3 = __builtin_bit_cast(float, __builtin_amdgcn_readlane(__builtin_bit_cast(int, m), 48));
;                 const float wm = fmaxf(fmaxf(r0, r1), fmaxf(r2, r3));
;                 const unsigned long long bal = __builtin_amdgcn_ballot_w64(v == wm);
;                 const int selL = (int)__builtin_ctzll(bal);
;                 ssum += __builtin_bit_cast(float, __builtin_amdgcn_readlane(__builtin_bit_cast(int, score), selL));
;                 if (lane == selL) { r = kk; v = -__builtin_inff(); }
	s_nop 0
	v_readlane_b32 s60, v149, 32
	v_readlane_b32 s61, v149, 48
	v_readlane_b32 s22, v149, 0
	v_readlane_b32 s23, v149, 16
	v_max_f32_e64 v149, s61, s61
	v_max_f32_e64 v150, s60, s60
	v_max_f32_e32 v149, v150, v149
	v_mov_b32_e32 v150, s23
	v_max3_f32 v149, s22, v150, v149
	v_cmp_eq_f32_e32 vcc, v147, v149
	s_ff1_i32_b64 s22, vcc
	v_cmp_eq_u32_e32 vcc, s22, v163
	v_readlane_b32 s60, v146, s22
	s_nop 0
	v_cndmask_b32_e32 v147, v147, v211, vcc
	v_max_f32_e32 v150, v147, v147
	v_cndmask_b32_e64 v148, v148, 6, vcc
	v_max_f32_dpp v149, v147, v150 quad_perm:[1,0,3,2] row_mask:0xf bank_mask:0xf bound_ctrl:1


; template <int CTRL> __device__ __forceinline__ float dppf(float x) { return __builtin_bit_cast(float, __builtin_amdgcn_update_dpp(0, __builtin_bit_cast(int, x), CTRL, 0xF, 0xF, true)); }
; __device__ __forceinline__ void p9_fused4(Frame& F) {
;     ...
;                 float m = v; m = fmaxf(m, dppf<0xB1>(m)); m = fmaxf(m, dppf<0x4E>(m)); m = fmaxf(m, dppf<0x141>(m)); m = fmaxf(m, dppf<0x140>(m));
	s_nop 1
	v_max_f32_dpp v149, v149, v149 quad_perm:[2,3,0,1] row_mask:0xf bank_mask:0xf bound_ctrl:1


; template <int CTRL> __device__ __forceinline__ float dppf(float x) { return __builtin_bit_cast(float, __builtin_amdgcn_update_dpp(0, __builtin_bit_cast(int, x), CTRL, 0xF, 0xF, true)); }
; __device__ __forceinline__ void p9_fused4(Frame& F) {
;     ...
;                 float m = v; m = fmaxf(m, dppf<0xB1>(m)); m = fmaxf(m, dppf<0x4E>(m)); m = fmaxf(m, dppf<0x141>(m)); m = fmaxf(m, dppf<0x140>(m));
	s_nop 1
	v_max_f32_dpp v149, v149, v149 row_half_mirror row_mask:0xf bank_mask:0xf bound_ctrl:1


; template <int CTRL> __device__ __forceinline__ float dppf(float x) { return __builtin_bit_cast(float, __builtin_amdgcn_update_dpp(0, __builtin_bit_cast(int, x), CTRL, 0xF, 0xF, true)); }
; __device__ __forceinline__ void p9_fused4(Frame& F) {
;     ...
;                 float m = v; m = fmaxf(m, dppf<0xB1>(m)); m = fmaxf(m, dppf<0x4E>(m)); m = fmaxf(m, dppf<0x141>(m)); m = fmaxf(m, dppf<0x140>(m));
	s_nop 1
	v_max_f32_dpp v149, v149, v149 row_mirror row_mask:0xf bank_mask:0xf bound_ctrl:1


; __device__ __forceinline__ void p9_fused4(Frame& F) {
;     ...
;                 const float r0 = __builtin_bit_cast(float, __builtin_amdgcn_readlane(__builtin_bit_cast(int, m), 0)), r1 = __builtin_bit_cast(float, __builtin_amdgcn_readlane(__builtin_bit_cast(int, m), 16));
;                 const float r2 = __builtin_bit_cast(float, __builtin_amdgcn_readlane(__builtin_bit_cast(int, m), 32)), r3 = __builtin_bit_cast(float, __builtin_amdgcn_readlane(__builtin_bit_cast(int, m), 48));
;                 const float wm = fmaxf(fmaxf(r0, r1), fmaxf(r2, r3));
;                 const unsigned long long bal = __builtin_amdgcn_ballot_w64(v == wm);
;                 const int selL = (int)__builtin_ctzll(bal);
;                 ssum += __builtin_bit_cast(float, __builtin_amdgcn_readlane(__builtin_bit_cast(int, score), selL));
;                 if (lane == selL) { r = kk; v = -__builtin_inff(); }
;             }
;             const bool sel = r < 8;
;             if (sel) { WSP(int, WS_EIDX)[(size_t)t * 8 + r] = lane; WSP(float, WS_EW)[(size_t)t * 8 + r] = score / ssum * 2.5f; if (rp_ == 0) atomicAdd((int*)&hist[lane], 1); }
	s_nop 0
	v_readlane_b32 s61, v149, 32
	v_readlane_b32 s62, v149, 48
	v_readlane_b32 s22, v149, 0
	v_readlane_b32 s23, v149, 16
	v_max_f32_e64 v149, s62, s62
	v_max_f32_e64 v150, s61, s61
	v_max_f32_e32 v149, v150, v149
	v_mov_b32_e32 v150, s23
	v_max3_f32 v149, s22, v150, v149
	v_cmp_eq_f32_e32 vcc, v147, v149
	s_ff1_i32_b64 s22, vcc
	v_cmp_ne_u32_e32 vcc, s22, v163
	v_readlane_b32 s61, v146, s22
	s_nop 0
	v_cndmask_b32_e32 v164, 7, v148, vcc
	v_cmp_gt_u32_e32 vcc, 8, v164
	s_and_saveexec_b64 s[22:23], vcc
	s_cbranch_execz .LBB0_1398
	v_add_f32_e64 v147, s24, 0
	v_add_f32_e32 v147, s25, v147
	v_add_f32_e32 v147, s56, v147
	v_add_f32_e32 v147, s57, v147
	v_add_f32_e32 v147, s58, v147
	v_add_f32_e32 v147, s59, v147
	v_add_f32_e32 v147, s60, v147
	v_add_f32_e32 v147, s61, v147
	s_lshl_b64 s[24:25], s[50:51], 5
	v_div_scale_f32 v152, s[50:51], v147, v147, v146
	v_rcp_f32_e32 v153, v152
	v_lshlrev_b64 v[148:149], 2, v[164:165]
	v_or_b32_e32 v149, s25, v149
	v_or_b32_e32 v148, s24, v148
	v_lshl_add_u64 v[150:151], s[46:47], 0, v[148:149]
	global_store_dword v[150:151], v163, off
	v_fma_f32 v150, -v152, v153, 1.0
	v_fmac_f32_e32 v153, v150, v153
	v_div_scale_f32 v150, vcc, v146, v147, v146
	v_mul_f32_e32 v151, v150, v153
	v_fma_f32 v154, -v152, v151, v150
	v_fmac_f32_e32 v151, v154, v153
	v_fma_f32 v150, -v152, v151, v150
	v_div_fmas_f32 v150, v150, v153, v151
	v_div_fixup_f32 v146, v150, v147, v146
	v_mul_f32_e32 v150, 0x40200000, v146
	v_lshl_add_u64 v[146:147], s[48:49], 0, v[148:149]
	global_store_dword v[146:147], v150, off
	ds_add_u32 v193, v209
	s_branch .LBB0_1398
